# v17 with run-time selection of the XCD-local barriers (used only if every workgroup saw XCC_ID == block&7 and the grid has 256 workgroups; else the original grid barriers)
# speedup vs baseline: 1.0533x; 1.0018x over previous
.LBB0_5:
	s_or_b64 exec, exec, s[0:1]
	s_load_dwordx4 s[0:3], s[80:81], 0x170
	v_cmp_eq_u32_e32 vcc, 0, v0
	s_waitcnt lgkmcnt(0)
	s_barrier
	s_sub_i32 s2, s3, s2
	s_cmp_lt_i32 s2, 2
	s_cselect_b64 s[4:5], -1, 0
	v_writelane_b32 v253, s4, 6
	s_add_u32 s0, s0, 0x4000
	s_addc_u32 s1, s1, 0
	v_writelane_b32 v253, s5, 7
	s_mov_b32 s3, 0
	s_cmp_gt_i32 s2, 1
	s_mov_b32 s2, 0
	v_writelane_b32 v253, s3, 8
	s_cbranch_scc0 .LBB0_10
	s_getreg_b32 s2, hwreg(HW_REG_XCC_ID, 0, 4)
	s_and_b32 s2, s2, 15
	s_and_saveexec_b64 s[4:5], vcc
	s_cbranch_execz .LBB0_9
	s_mov_b64 s[6:7], exec
	v_mbcnt_lo_u32_b32 v1, s6, 0
	v_mbcnt_hi_u32_b32 v1, s7, v1
	v_cmp_eq_u32_e32 vcc, 0, v1
	s_and_b64 s[8:9], exec, vcc
	s_mov_b64 exec, s[8:9]
	s_cbranch_execz .LBB0_9
	s_lshl_b32 s3, s2, 8
	s_bcnt1_i32_b64 s6, s[6:7]
	v_mov_b32_e32 v1, s3
	v_mov_b32_e32 v2, s6
	global_atomic_add v1, v2, s[0:1] offset:1024
	s_and_b32 s3, s92, 7
	s_cmp_lg_u32 s3, s2
	s_cselect_b32 s3, 1, 0
	s_cmpk_lg_u32 s91, 0x100
	s_cselect_b32 s6, 1, 0
	s_or_b32 s3, s3, s6
	s_cmp_eq_u32 s3, 0
	s_cbranch_scc1 .Lxm_ok
	v_mov_b32_e32 v1, 0
	v_mov_b32_e32 v2, 1
	global_atomic_add v1, v2, s[0:1] offset:256
.Lxm_ok:
.LBB0_9:
	s_or_b64 exec, exec, s[4:5]
	s_add_i32 s3, 0, 0x20000
	v_writelane_b32 v253, s3, 8

.LBB0_721:
	s_mov_b32 s4, 0
	s_nop 0
	v_writelane_b32 v255, s4, 49
	s_load_dwordx2 s[4:5], s[80:81], 0x170
	v_mov_b32_e32 v1, 0x4100
	s_waitcnt lgkmcnt(0)
	global_load_dword v1, v1, s[4:5] sc1
	s_waitcnt vmcnt(0)
	v_readfirstlane_b32 s4, v1
	s_nop 3
	s_cmp_eq_u32 s4, 0
	s_cselect_b32 s4, 1, 0
	s_nop 0
	v_writelane_b32 v255, s4, 50
	s_mov_b32 s4, 0
	s_nop 0
	v_writelane_b32 v255, s4, 42
	s_cmpk_lt_i32 s92, 0x400
	s_cselect_b64 s[4:5], -1, 0
	s_ashr_i32 s83, s92, 31
	v_writelane_b32 v253, s4, 11
	s_lshr_b32 s3, s83, 29
	s_mov_b32 s35, 0
	v_writelane_b32 v253, s5, 12
	s_add_i32 s4, s92, s3
	s_ashr_i32 s3, s4, 3
	s_and_b32 s4, s4, -8
	s_sub_i32 s4, s92, s4
	s_lshl_b32 s5, s4, 7
	s_cmpk_lt_i32 s92, 0x700
	s_cselect_b64 s[6:7], -1, 0
	v_writelane_b32 v253, s6, 13
	v_mov_b32_e32 v65, 0
	s_mov_b64 s[88:89], 0x80
	v_writelane_b32 v253, s7, 14
	s_mov_b32 s95, 0x437f0000
	v_readlane_b32 s8, v253, 2
	v_readlane_b32 s9, v253, 3
	s_add_u32 s6, s8, 0x4200
	s_addc_u32 s7, s9, 0
	v_readlane_b32 s10, v253, 4
	v_readlane_b32 s11, v253, 5
	v_writelane_b32 v253, s6, 15
	v_mov_b32_e32 v167, 1
	s_mov_b32 s28, 0x800000
	v_writelane_b32 v253, s7, 16
	s_add_u32 s6, s8, 0x4400
	s_addc_u32 s7, s9, 0
	v_writelane_b32 v253, s6, 17
	s_movk_i32 s31, 0x240
	s_mov_b32 s29, 0xf800000
	v_writelane_b32 v253, s7, 18
	s_add_u32 s6, s8, 0x4500
	s_addc_u32 s7, s9, 0
	v_writelane_b32 v253, s6, 19
	v_mov_b32_e32 v214, 0x260
	s_mov_b32 s94, 0xbf1b4598
	v_writelane_b32 v253, s7, 20
	s_add_u32 s6, s8, 0x4600
	s_addc_u32 s7, s9, 0
	v_writelane_b32 v253, s6, 21
	s_movk_i32 s30, 0x7fff
	v_mov_b32_e32 v215, 0xff61b1e6
	v_writelane_b32 v253, s7, 22
	s_add_u32 s6, s8, 0x4700
	s_addc_u32 s7, s9, 0
	v_writelane_b32 v253, s6, 23
	v_mov_b32_e32 v216, 8
	s_mov_b32 s36, 0x42800000
	v_writelane_b32 v253, s7, 24
	s_add_u32 s6, s8, 0x4800
	s_addc_u32 s7, s9, 0
	v_writelane_b32 v253, s6, 25
	v_mov_b32_e32 v217, 0x3a27c5ac
	v_mov_b32_e32 v218, 0x3727c5ac
	v_writelane_b32 v253, s7, 26
	s_add_u32 s6, s8, 0x4900
	s_addc_u32 s7, s9, 0
	v_writelane_b32 v253, s6, 27
	s_mov_b32 s90, 0xc0e00000
	v_mov_b64_e32 v[250:251], 0x6ff
	v_writelane_b32 v253, s7, 28
	s_add_u32 s6, s8, 0x4a00
	s_addc_u32 s7, s9, 0
	v_writelane_b32 v253, s6, 29
	v_mov_b32_e32 v219, 0x41b17218
	v_mov_b32_e32 v252, 0x7ff
	v_writelane_b32 v253, s7, 30
	s_add_u32 s6, s8, 0x4b00
	s_addc_u32 s7, s9, 0
	v_writelane_b32 v253, s6, 31
	v_mov_b32_e32 v224, 0xffffa800
	v_mov_b32_e32 v225, 0x43e00000
	v_writelane_b32 v253, s7, 32
	s_add_u32 s6, s8, 0x4c00
	s_addc_u32 s7, s9, 0
	v_writelane_b32 v253, s6, 33
	v_mov_b32_e32 v166, 0x358637bd
	v_mov_b64_e32 v[168:169], 0x100
	v_writelane_b32 v253, s7, 34
	s_add_u32 s6, s8, 0x4d00
	s_addc_u32 s7, s9, 0
	v_writelane_b32 v253, s6, 35
	v_mov_b64_e32 v[170:171], 0xff
	v_mov_b32_e32 v226, 0x40e00000
	v_writelane_b32 v253, s7, 36
	s_add_u32 s6, s8, 0x4e00
	s_addc_u32 s7, s9, 0
	v_writelane_b32 v253, s6, 37
	s_nop 1
	v_writelane_b32 v253, s7, 38
	s_add_u32 s6, s8, 0x4f00
	s_addc_u32 s7, s9, 0
	v_writelane_b32 v253, s6, 39
	s_nop 1
	v_writelane_b32 v253, s7, 40
	s_add_u32 s6, s8, 0x5000
	s_addc_u32 s7, s9, 0
	v_writelane_b32 v253, s6, 41
	s_nop 1
	v_writelane_b32 v253, s7, 42
	s_add_u32 s6, s8, 0x5100
	s_addc_u32 s7, s9, 0
	v_writelane_b32 v253, s6, 43
	s_nop 1
	v_writelane_b32 v253, s7, 44
	s_add_u32 s6, s8, 0x5200
	s_addc_u32 s7, s9, 0
	v_writelane_b32 v253, s6, 45
	s_nop 1
	v_writelane_b32 v253, s7, 46
	s_add_u32 s6, s8, 0x5300
	s_addc_u32 s7, s9, 0
	v_writelane_b32 v253, s6, 47
	s_cmp_eq_u32 s2, 15
	s_nop 0
	v_writelane_b32 v253, s7, 48
	s_cselect_b64 s[6:7], -1, 0
	v_writelane_b32 v253, s6, 49
	s_cmp_eq_u32 s2, 14
	s_nop 0
	v_writelane_b32 v253, s7, 50
	s_cselect_b64 s[6:7], -1, 0
	v_writelane_b32 v253, s6, 51
	s_cmp_eq_u32 s2, 13
	s_nop 0
	v_writelane_b32 v253, s7, 52
	s_cselect_b64 s[6:7], -1, 0
	v_writelane_b32 v253, s6, 53
	s_cmp_eq_u32 s2, 12
	s_nop 0
	v_writelane_b32 v253, s7, 54
	s_cselect_b64 s[6:7], -1, 0
	v_writelane_b32 v253, s6, 55
	s_cmp_eq_u32 s2, 11
	s_nop 0
	v_writelane_b32 v253, s7, 56
	s_cselect_b64 s[6:7], -1, 0
	v_writelane_b32 v253, s6, 57
	s_cmp_eq_u32 s2, 10
	s_nop 0
	v_writelane_b32 v253, s7, 58
	s_cselect_b64 s[6:7], -1, 0
	v_writelane_b32 v253, s6, 59
	s_cmp_eq_u32 s2, 9
	s_nop 0
	v_writelane_b32 v253, s7, 60
	s_cselect_b64 s[6:7], -1, 0
	v_writelane_b32 v253, s6, 61
	s_cmp_eq_u32 s2, 8
	s_nop 0
	v_writelane_b32 v253, s7, 62
	s_cselect_b64 s[6:7], -1, 0
	v_writelane_b32 v253, s6, 63
	s_cmp_eq_u32 s2, 7
	s_nop 0
	v_writelane_b32 v254, s7, 0
	s_cselect_b64 s[6:7], -1, 0
	v_writelane_b32 v254, s6, 1
	s_cmp_eq_u32 s2, 6
	s_nop 0
	v_writelane_b32 v254, s7, 2
	s_cselect_b64 s[6:7], -1, 0
	v_writelane_b32 v254, s6, 3
	s_cmp_eq_u32 s2, 5
	s_nop 0
	v_writelane_b32 v254, s7, 4
	s_cselect_b64 s[6:7], -1, 0
	v_writelane_b32 v254, s6, 5
	s_cmp_eq_u32 s2, 4
	s_nop 0
	v_writelane_b32 v254, s7, 6
	s_cselect_b64 s[6:7], -1, 0
	v_writelane_b32 v254, s6, 7
	s_cmp_eq_u32 s2, 3
	s_nop 0
	v_writelane_b32 v254, s7, 8
	s_cselect_b64 s[6:7], -1, 0
	v_writelane_b32 v254, s6, 9
	s_cmp_eq_u32 s2, 2
	s_nop 0
	v_writelane_b32 v254, s7, 10
	s_cselect_b64 s[6:7], -1, 0
	v_writelane_b32 v254, s6, 11
	s_cmp_eq_u32 s2, 1
	s_nop 0
	v_writelane_b32 v254, s7, 12
	s_cselect_b64 s[6:7], -1, 0
	v_writelane_b32 v254, s6, 13
	s_cmp_eq_u32 s2, 0
	s_nop 0
	v_writelane_b32 v254, s7, 14
	s_cselect_b64 s[6:7], -1, 0
	s_lshl_b32 s2, s2, 8
	s_add_u32 s0, s0, s2
	v_writelane_b32 v254, s6, 15
	s_addc_u32 s1, s1, 0
	s_mul_i32 s2, s4, 33
	v_writelane_b32 v254, s7, 16
	s_add_u32 s6, s0, 0x1400
	s_addc_u32 s7, s1, 0
	v_writelane_b32 v254, s6, 17
	s_add_u32 s0, s0, 0x2400
	s_addc_u32 s1, s1, 0
	v_writelane_b32 v254, s7, 18
	v_writelane_b32 v254, s0, 19
	v_cmp_eq_u32_e64 s[6:7], 0, v0
	s_nop 0
	v_writelane_b32 v254, s1, 20
	s_add_u32 s0, s8, 0x7400
	s_addc_u32 s1, s9, 0
	v_writelane_b32 v254, s0, 21
	s_nop 1
	v_writelane_b32 v254, s1, 22
	s_add_u32 s0, s8, 0x7500
	s_addc_u32 s1, s9, 0
	v_writelane_b32 v254, s0, 23
	s_cmpk_lt_i32 s92, 0x100
	s_nop 0
	v_writelane_b32 v254, s1, 24
	s_cselect_b64 s[0:1], -1, 0
	v_writelane_b32 v254, s0, 25
	s_nop 1
	v_writelane_b32 v254, s1, 26
	s_lshl_b32 s0, s4, 5
	s_cmp_lt_i32 s4, 0
	s_mul_i32 s1, s4, 0x81
	s_cselect_b32 s1, s1, s5
	s_movk_i32 s5, 0xe1
	s_cselect_b32 s5, s5, 0xe0
	s_cselect_b32 s2, s2, s0
	s_add_i32 s0, s1, s3
	s_ashr_i32 s1, s0, 31
	s_lshr_b32 s1, s1, 25
	v_writelane_b32 v254, s6, 27
	s_add_i32 s1, s0, s1
	s_add_i32 s84, 0, 0x14a00
	v_writelane_b32 v254, s7, 28
	s_ashr_i32 s6, s1, 7
	s_and_b32 s1, s1, 0xff80
	s_sub_i32 s1, s0, s1
	s_bfe_i32 s0, s1, 0x80000
	s_bfe_u32 s0, s0, 0x3000c
	s_add_i32 s7, s1, s0
	s_bfe_i32 s0, s7, 0x80000
	s_and_b32 s7, s7, 0xf8
	s_sub_i32 s1, s1, s7
	s_lshl_b32 s6, s6, 3
	s_sext_i32_i16 s8, s0
	s_sext_i32_i8 s1, s1
	s_add_i32 s10, s6, s1
	s_ashr_i32 s1, s8, 3
	v_writelane_b32 v254, s1, 29
	s_mov_b32 s6, s10
	s_ashr_i32 s11, s10, 31
	v_writelane_b32 v254, s6, 30
	s_lshr_b32 s0, s8, 3
	s_bfe_i64 s[0:1], s[0:1], 0x100000
	v_writelane_b32 v254, s7, 31
	s_lshl_b64 s[6:7], s[10:11], 18
	v_writelane_b32 v254, s6, 32
	s_lshl_b64 s[0:1], s[0:1], 18
	s_add_i32 s85, 0, 0x15200
	v_writelane_b32 v254, s7, 33
	v_writelane_b32 v254, s0, 34
	s_add_i32 s37, 0, 0x15a00
	s_add_i32 s96, 0, 0x16200
	v_writelane_b32 v254, s1, 35
	s_mul_i32 s0, s4, s5
	s_add_i32 s0, s0, s3
	s_mul_hi_i32 s1, s0, 0x92492493
	s_add_i32 s1, s1, s0
	s_lshr_b32 s4, s1, 31
	s_ashr_i32 s1, s1, 7
	s_add_i32 s1, s1, s4
	s_mul_i32 s4, s1, 0xe0
	s_sub_i32 s4, s0, s4
	s_bfe_u32 s0, s4, 0x3001c
	s_add_i32 s5, s4, s0
	s_sext_i32_i16 s6, s5
	s_and_b32 s5, s5, 0xfff8
	s_sub_i32 s4, s4, s5
	s_lshl_b32 s1, s1, 3
	s_sext_i32_i16 s4, s4
	s_add_i32 s8, s1, s4
	s_ashr_i32 s1, s6, 3
	v_writelane_b32 v254, s1, 36
	s_add_i32 s1, s2, s3
	s_ashr_i32 s2, s1, 31
	s_lshr_b32 s2, s2, 27
	s_add_i32 s2, s1, s2
	s_ashr_i32 s3, s2, 5
	s_and_b32 s2, s2, 0xffe0
	s_sub_i32 s1, s1, s2
	s_bfe_i32 s2, s1, 0x80000
	s_bfe_u32 s2, s2, 0x3000c
	s_add_i32 s4, s1, s2
	s_bfe_i32 s2, s4, 0x80000
	s_and_b32 s4, s4, 0xf8
	s_sub_i32 s1, s1, s4
	s_lshl_b32 s3, s3, 3
	s_sext_i32_i8 s1, s1
	s_lshr_b32 s0, s6, 3
	s_sext_i32_i16 s5, s2
	s_add_i32 s6, s3, s1
	s_lshr_b32 s2, s5, 3
	s_ashr_i32 s5, s5, 3
	s_ashr_i32 s7, s6, 31
	v_writelane_b32 v254, s5, 37
	s_lshl_b64 s[4:5], s[6:7], 18
	v_writelane_b32 v254, s4, 38
	s_bfe_i64 s[2:3], s[2:3], 0x100000
	s_ashr_i32 s9, s8, 31
	v_writelane_b32 v254, s5, 39
	s_lshl_b64 s[4:5], s[2:3], 18
	v_writelane_b32 v254, s4, 40
	s_bfe_i64 s[0:1], s[0:1], 0x100000
	s_lshl_b64 s[0:1], s[0:1], 19
	v_writelane_b32 v254, s5, 41
	s_mov_b32 s4, s8
	v_writelane_b32 v254, s4, 42
	s_add_i32 s97, 0, 0x16a00
	s_nop 0
	v_writelane_b32 v254, s5, 43
	s_lshl_b64 s[4:5], s[8:9], 19
	v_writelane_b32 v254, s4, 44
	s_nop 1
	v_writelane_b32 v254, s5, 45
	v_writelane_b32 v254, s0, 46
	s_add_i32 s4, 0, 0x20040
	s_nop 0
	v_writelane_b32 v254, s1, 47
	s_mov_b32 s0, s6
	v_writelane_b32 v254, s0, 48
	s_nop 1
	v_writelane_b32 v254, s1, 49
	s_lshl_b64 s[0:1], s[6:7], 17
	v_writelane_b32 v254, s0, 50
	s_mov_b32 s6, s35
	s_nop 0
	v_writelane_b32 v254, s1, 51
	s_lshl_b64 s[0:1], s[2:3], 17
	v_writelane_b32 v254, s0, 52
	s_add_i32 s2, 0, 0x10400
	s_mov_b32 s3, 0xc3e00000
	v_writelane_b32 v254, s1, 53
	s_mov_b64 s[0:1], 0
	v_writelane_b32 v254, s0, 54
	s_nop 1
	v_writelane_b32 v254, s1, 55
	s_add_i32 s0, 0, 0x11a00
	v_writelane_b32 v254, s0, 56
	s_add_i32 s0, 0, 0x17210
	v_writelane_b32 v254, s0, 57
	s_add_i32 s0, 0, 0x13000
	v_writelane_b32 v254, s0, 58
	s_add_i32 s0, 0, 0x20780
	v_writelane_b32 v254, s0, 59
	v_writelane_b32 v254, s2, 60
	s_add_i32 s2, 0, 0x20640
	v_writelane_b32 v254, s2, 61
	v_writelane_b32 v254, s4, 62
	s_add_i32 s4, 0, 0x20600
	v_writelane_b32 v254, s4, 63
	s_add_i32 s4, 0, 0x20740
	v_writelane_b32 v255, s4, 0
	v_writelane_b32 v255, s83, 1
	v_writelane_b32 v255, s92, 2
	s_movk_i32 s1, 0x5800
	s_mov_b32 s0, 0x3d808081
	s_add_i32 s2, 0, 0x206c0
	v_writelane_b32 v255, s86, 3
	s_branch .LBB0_725

.LBB0_795:
	s_andn2_saveexec_b64 s[6:7], s[6:7]
	s_cbranch_execz .LBB0_813
	s_mov_b64 s[6:7], exec
	v_readlane_b32 s8, v255, 50
	s_nop 3
	s_cmp_eq_u32 s8, 1
	s_cbranch_scc0 .Lxg_814
	s_waitcnt lgkmcnt(0)
	s_branch .Lxl_814
.Lxg_814:
	buffer_wbl2 sc1
	s_waitcnt lgkmcnt(0)
	s_waitcnt vmcnt(0)
	v_mbcnt_lo_u32_b32 v1, s6, 0
	v_mbcnt_hi_u32_b32 v1, s7, v1
	v_cmp_eq_u32_e32 vcc, 0, v1
	s_and_saveexec_b64 s[8:9], vcc
	s_cbranch_execz .LBB0_798
	s_bcnt1_i32_b64 s6, s[6:7]
	v_mov_b32_e32 v2, s6
	v_readlane_b32 s6, v254, 21
	v_readlane_b32 s7, v254, 22
	s_nop 4
	global_atomic_add v2, v65, v2, s[6:7] sc0

.LBB0_2492:
	s_lshl_b32 s20, s91, 3
	s_abs_i32 s7, s20
	v_cvt_f32_u32_e32 v1, s7
	s_lshl_b32 s6, s93, 3
	s_add_i32 s6, s6, s82
	s_sub_i32 s8, s20, s6
	v_rcp_iflag_f32_e32 v1, v1
	s_add_i32 s12, s8, 0x3fff
	s_sub_i32 s8, 0xffffc001, s8
	s_xor_b32 s13, s12, s20
	v_mul_f32_e32 v1, 0x4f7ffffe, v1
	v_cvt_u32_f32_e32 v1, v1
	s_sub_i32 s9, 0, s7
	s_max_i32 s8, s12, s8
	s_ashr_i32 s12, s13, 31
	v_readfirstlane_b32 s13, v1
	s_mul_i32 s9, s9, s13
	s_mul_hi_u32 s9, s13, s9
	s_add_i32 s13, s13, s9
	s_mul_hi_u32 s9, s8, s13
	s_mul_i32 s13, s9, s7
	s_sub_i32 s8, s8, s13
	s_add_i32 s13, s9, 1
	s_sub_i32 s14, s8, s7
	s_cmp_ge_u32 s8, s7
	s_cselect_b32 s9, s13, s9
	s_cselect_b32 s8, s14, s8
	s_add_i32 s13, s9, 1
	s_cmp_ge_u32 s8, s7
	s_cselect_b32 s7, s13, s9
	s_xor_b32 s7, s7, s12
	s_sub_i32 s21, s7, s12
	s_cmpk_lg_u32 s91, 0x100
	s_cbranch_scc1 .Lcomb_nomap
	s_lshr_b32 s7, s93, 5
	s_and_b32 s8, s93, 31
	s_lshl_b32 s7, s7, 11
	s_lshl_b32 s8, s8, 3
	s_add_i32 s6, s7, s8
	s_add_i32 s6, s6, s82
	s_movk_i32 s20, 0x100
	s_mov_b32 s21, 8
.Lcomb_nomap:
	s_cmp_lt_i32 s21, 1
	s_cbranch_scc1 .LBB0_2501
	s_waitcnt lgkmcnt(0)
	s_add_u32 s14, s10, 0x8a200000
	s_addc_u32 s15, s11, 0
	s_add_u32 s22, s10, 0x8c500000
	s_load_dwordx4 s[24:27], s[4:5], 0x158
	s_addc_u32 s23, s11, 0
	s_add_u32 s16, s10, 0xa7600000
	v_readlane_b32 s38, v255, 4
	s_addc_u32 s17, s11, 0
	s_lshl_b32 s34, s38, 10
	s_lshl_b64 s[8:9], s[34:35], 2
	s_waitcnt lgkmcnt(0)
	s_add_u32 s12, s24, s8
	s_addc_u32 s13, s25, s9
	s_add_u32 s8, s26, s8
	s_addc_u32 s9, s27, s9
	v_lshlrev_b32_e32 v52, 2, v0
	v_ashrrev_i32_e32 v53, 31, v52
	s_add_u32 s24, s10, 0x8c400000
	v_lshlrev_b64 v[0:1], 2, v[52:53]
	s_addc_u32 s25, s11, 0
	v_lshl_add_u64 v[28:29], s[8:9], 0, v[0:1]
	s_add_u32 s8, s10, 0x9e600000
	v_lshlrev_b64 v[32:33], 1, v[52:53]
	v_lshl_add_u64 v[24:25], s[12:13], 0, v[0:1]
	s_addc_u32 s9, s11, 0
	v_lshl_add_u64 v[34:35], s[10:11], 0, v[32:33]
	s_mov_b64 s[12:13], 0x42000000
	s_ashr_i32 s7, s6, 31
	v_lshl_add_u64 v[58:59], v[34:35], 0, s[12:13]
	s_lshl_b64 s[12:13], s[6:7], 4
	s_add_u32 s18, s24, s12
	s_addc_u32 s19, s25, s13
	global_load_dwordx4 v[0:3], v[24:25], off
	global_load_dwordx4 v[4:7], v[28:29], off
	global_load_dwordx4 v[8:11], v[24:25], off offset:1024
	global_load_dwordx4 v[12:15], v[28:29], off offset:1024
	global_load_dwordx4 v[16:19], v[24:25], off offset:2048
	global_load_dwordx4 v[20:23], v[28:29], off offset:2048
	s_nop 0
	global_load_dwordx4 v[24:27], v[24:25], off offset:3072
	s_nop 0
	global_load_dwordx4 v[28:31], v[28:29], off offset:3072
	v_lshl_add_u64 v[56:57], s[16:17], 0, v[32:33]
	global_load_dwordx4 v[34:37], v65, s[18:19]
	v_lshl_add_u64 v[54:55], s[14:15], 0, v[32:33]
	v_lshl_add_u64 v[60:61], s[10:11], 0, v[52:53]
	s_mov_b64 s[10:11], 0x8c600000
	v_lshl_add_u64 v[62:63], v[60:61], 0, s[10:11]
	v_readlane_b32 s39, v255, 5
	s_waitcnt vmcnt(0)
	v_readfirstlane_b32 s33, v37
	s_lshr_b32 s26, s33, 18
	s_and_b32 s34, s26, 0x3ffc
	s_add_i32 s26, 0, 0x20000
	s_add_i32 s34, s26, s34
	v_readfirstlane_b32 s18, v34
	v_mov_b32_e32 v34, s34
	ds_read_b32 v64, v34 offset:1408
	v_readfirstlane_b32 s19, v35
	v_readfirstlane_b32 s27, v36
	s_lshl_b32 s33, s33, 10
	s_and_b32 s34, s33, 0x3ffffc00
	s_waitcnt lgkmcnt(0)
	v_lshlrev_b64 v[34:35], 18, v[64:65]
	v_lshl_add_u64 v[34:35], s[8:9], 0, v[34:35]
	s_lshr_b32 s33, s27, 18
	v_lshl_add_u64 v[34:35], v[34:35], 0, s[34:35]
	s_and_b32 s33, s33, 0x3ffc
	v_lshl_add_u64 v[34:35], v[34:35], 0, v[52:53]
	s_add_i32 s33, s26, s33
	global_load_dword v94, v[34:35], off offset:768 nt
	global_load_dword v95, v[34:35], off offset:512 nt
	global_load_dword v96, v[34:35], off offset:256 nt
	global_load_dword v97, v[34:35], off nt
	v_mov_b32_e32 v34, s33
	ds_read_b32 v64, v34 offset:1408
	s_lshl_b32 s27, s27, 10
	s_and_b32 s34, s27, 0x3ffffc00
	s_lshr_b32 s27, s19, 18
	s_and_b32 s27, s27, 0x3ffc
	s_waitcnt lgkmcnt(0)
	v_lshlrev_b64 v[34:35], 18, v[64:65]
	v_lshl_add_u64 v[34:35], s[8:9], 0, v[34:35]
	v_lshl_add_u64 v[34:35], v[34:35], 0, s[34:35]
	v_lshl_add_u64 v[34:35], v[34:35], 0, v[52:53]
	s_add_i32 s27, s26, s27
	global_load_dword v98, v[34:35], off offset:768 nt
	global_load_dword v99, v[34:35], off offset:512 nt
	global_load_dword v100, v[34:35], off offset:256 nt
	global_load_dword v101, v[34:35], off nt
	v_mov_b32_e32 v34, s27
	ds_read_b32 v64, v34 offset:1408
	s_lshl_b32 s19, s19, 10
	s_and_b32 s34, s19, 0x3ffffc00
	s_lshr_b32 s19, s18, 18
	s_and_b32 s19, s19, 0x3ffc
	s_waitcnt lgkmcnt(0)
	v_lshlrev_b64 v[34:35], 18, v[64:65]
	v_lshl_add_u64 v[34:35], s[8:9], 0, v[34:35]
	v_lshl_add_u64 v[34:35], v[34:35], 0, s[34:35]
	v_lshl_add_u64 v[34:35], v[34:35], 0, v[52:53]
	s_add_i32 s19, s26, s19
	global_load_dword v102, v[34:35], off offset:768 nt
	global_load_dword v103, v[34:35], off offset:512 nt
	global_load_dword v104, v[34:35], off offset:256 nt
	global_load_dword v105, v[34:35], off nt
	v_mov_b32_e32 v34, s19
	ds_read_b32 v64, v34 offset:1408
	s_lshl_b32 s18, s18, 10
	s_and_b32 s34, s18, 0x3ffffc00
	s_lshl_b64 s[18:19], s[6:7], 11
	s_add_u32 s16, s16, s18
	s_waitcnt lgkmcnt(0)
	v_lshlrev_b64 v[34:35], 18, v[64:65]
	s_addc_u32 s17, s17, s19
	v_lshl_add_u64 v[34:35], s[8:9], 0, v[34:35]
	s_add_u32 s14, s14, s18
	v_lshl_add_u64 v[34:35], v[34:35], 0, s[34:35]
	s_addc_u32 s15, s15, s19
	v_lshl_add_u64 v[34:35], v[34:35], 0, v[52:53]
	s_cmp_lg_u32 s21, 1
	global_load_dword v106, v[34:35], off offset:768 nt
	global_load_dword v107, v[34:35], off offset:512 nt
	global_load_dword v108, v[34:35], off offset:256 nt
	global_load_dword v109, v[34:35], off nt
	v_lshl_add_u64 v[34:35], s[16:17], 0, v[32:33]
	v_lshl_add_u64 v[32:33], s[14:15], 0, v[32:33]
	s_cselect_b32 s14, s20, 0
	s_add_i32 s14, s14, s6
	s_ashr_i32 s15, s14, 31
	s_lshl_b64 s[14:15], s[14:15], 4
	s_add_u32 s16, s22, s14
	s_addc_u32 s17, s23, s15
	s_add_u32 s14, s24, s14
	s_addc_u32 s15, s25, s15
	global_load_dwordx2 v[44:45], v[34:35], off offset:1536 nt
	global_load_dwordx2 v[46:47], v[32:33], off offset:1536 nt
	global_load_dwordx2 v[48:49], v[34:35], off offset:1024 nt
	global_load_dwordx2 v[50:51], v[32:33], off offset:1024 nt
	global_load_dwordx2 v[86:87], v[34:35], off offset:512 nt
	global_load_dwordx2 v[88:89], v[32:33], off offset:512 nt
	global_load_dwordx2 v[90:91], v[34:35], off nt
	global_load_dwordx2 v[92:93], v[32:33], off nt
	global_load_dwordx4 v[36:39], v65, s[14:15]
	s_add_u32 s12, s22, s12
	global_load_dwordx4 v[32:35], v65, s[16:17]
	s_addc_u32 s13, s23, s13
	s_cmp_lg_u32 s38, 3
	s_mov_b32 s7, 0
	s_waitcnt vmcnt(1)
	v_readfirstlane_b32 s16, v39
	v_readfirstlane_b32 s17, v38
	v_readfirstlane_b32 s18, v37
	v_readfirstlane_b32 s19, v36
	global_load_dwordx4 v[36:39], v65, s[12:13]
	s_cselect_b64 s[12:13], -1, 0
	s_lshl_b32 s14, s20, 1
	s_branch .LBB0_2495

.LBB0_2533:
	s_mov_b64 s[6:7], exec
	v_readlane_b32 s8, v255, 50
	s_nop 3
	s_cmp_eq_u32 s8, 1
	s_cbranch_scc0 .Lxg_last
	s_waitcnt lgkmcnt(0)
	s_branch .Lxl_last

.Lxl_last:
	s_getpc_b64 s[98:99]
